# Y/z private buffers remapped to lane-linear layout (1KB contiguous per wave access) in G2 stores + G3 yv/za/zb loads + in-place z stores; based on v6 + sc1 loads
# speedup vs baseline: 1.0124x; 1.0124x over previous
; __device__ __forceinline__ unsigned pk2h(float lo, float hi) { f32x2 v = {lo, hi}; f16x2 h = __builtin_convertvector(v, f16x2); return __builtin_bit_cast(unsigned, h); }
;     __device__ __forceinline__ void operator()(const f32x4 (&acc)[2][2][4][2], const Unit& u, int wr, int wc, int fr, int fq) const {
;         const int row0 = u.pm * BM + wr * 64 + fr; const int col0 = u.pn * BM + wc * 32 + 8 * fq;
; #pragma unroll
;         for (int ai = 0; ai < 2; ++ai)
; #pragma unroll
;             for (int m = 0; m < 4; ++m) { f16* rowp = O + (size_t)(row0 + ai * HALF + m * 16) * ldc + (size_t)((row0 + ai * HALF + m * 16) >> 12) * gap + col0;
; #pragma unroll
;                 for (int bj = 0; bj < 2; ++bj) { f32x4 v0 = acc[ai][bj][m][0], v1 = acc[ai][bj][m][1];
;                     if (ACT == 1) {
; #pragma unroll
;                         for (int e = 0; e < 4; ++e) { const float a = fmaxf(v0[e], 0.f), b = fmaxf(v1[e], 0.f); v0[e] = a * a; v1[e] = b * b; } }
;                     u32x4 w; w.x = pk2h(v0[0], v0[1]); w.y = pk2h(v0[2], v0[3]); w.z = pk2h(v1[0], v1[1]); w.w = pk2h(v1[2], v1[3]);
;                     gst16(rowp + bj * HALF, w); } }
.LBB0_1135:
	s_lshl_b32 s38, s53, 8
	s_add_i32 s38, s38, s96
	v_or_b32_e32 v138, s38, v133
	v_lshl_add_u32 v140, s52, 8, v136
	v_and_b32_e32 v139, 15, v138
	v_lshlrev_b32_e32 v139, 4, v139
	v_bfe_u32 v141, v140, 3, 2
	v_lshl_or_b32 v139, v141, 8, v139
	v_bfe_u32 v141, v140, 5, 2
	v_lshl_or_b32 v139, v141, 14, v139
	v_bfe_u32 v141, v138, 6, 1
	v_lshl_or_b32 v139, v141, 16, v139
	v_lshrrev_b32_e32 v141, 8, v140
	v_lshl_add_u32 v139, v141, 17, v139
	v_lshrrev_b32_e32 v141, 8, v138
	v_lshl_add_u32 v139, v141, 19, v139
	v_lshrrev_b32_e32 v141, 12, v138
	v_mul_u32_u24_e32 v141, 3, v141
	v_lshl_add_u32 v139, v141, 23, v139
	v_mov_b32_e32 v144, v139
	v_mov_b32_e32 v145, 0
	v_lshl_add_u64 v[144:145], s[40:41], 0, v[144:145]
	v_add_co_u32_e32 v142, vcc, 0x1000, v144
	s_nop 0
	v_addc_co_u32_e32 v143, vcc, 0, v145, vcc
	v_add_co_u32_e32 v140, vcc, 0x2000, v144
	s_nop 0
	v_addc_co_u32_e32 v141, vcc, 0, v145, vcc
	v_add_co_u32_e32 v138, vcc, 0x3000, v144
	s_nop 0
	v_addc_co_u32_e32 v139, vcc, 0, v145, vcc
	v_cvt_pk_f16_f32 v70, v70, v71
	v_cvt_pk_f16_f32 v71, v72, v73
	v_cvt_pk_f16_f32 v72, v66, v67
	v_cvt_pk_f16_f32 v110, v110, v111
	v_cvt_pk_f16_f32 v111, v112, v113
	v_cvt_pk_f16_f32 v112, v106, v107
	v_cvt_pk_f16_f32 v94, v94, v95
	v_cvt_pk_f16_f32 v95, v96, v97
	v_cvt_pk_f16_f32 v96, v90, v91
	v_cvt_pk_f16_f32 v78, v78, v79
	v_cvt_pk_f16_f32 v79, v80, v81
	v_cvt_pk_f16_f32 v80, v74, v75
	v_cvt_pk_f16_f32 v73, v68, v69
	s_ashr_i32 s42, s38, 12
	v_cvt_pk_f16_f32 v46, v46, v47
	v_cvt_pk_f16_f32 v47, v48, v49
	v_cvt_pk_f16_f32 v48, v42, v43
	v_cvt_pk_f16_f32 v49, v44, v45
	global_store_dwordx4 v[140:141], v[46:49], off offset:1024
	s_mov_b64 s[38:39], 0x48000
	v_cvt_pk_f16_f32 v44, v50, v51
	s_mov_b32 s38, 0x48000
	v_cvt_pk_f16_f32 v30, v30, v31
	v_cvt_pk_f16_f32 v31, v32, v33
	v_cvt_pk_f16_f32 v32, v26, v27
	v_cvt_pk_f16_f32 v33, v28, v29
	s_mov_b64 s[38:39], 0x50000
	global_store_dwordx4 v[140:141], v[30:33], off offset:3072
	v_cvt_pk_f16_f32 v14, v14, v15
	v_cvt_pk_f16_f32 v15, v16, v17
	s_mov_b32 s38, 0x50000
	v_cvt_pk_f16_f32 v16, v10, v11
	v_cvt_pk_f16_f32 v17, v12, v13
	s_mov_b64 s[38:39], 0x58000
	v_cvt_pk_f16_f32 v113, v108, v109
	global_store_dwordx4 v[138:139], v[14:17], off offset:1024
	global_store_dwordx4 v[144:145], v[110:113], off offset:1024
	v_cvt_pk_f16_f32 v97, v92, v93
	s_mov_b32 s38, 0x58000
	global_store_dwordx4 v[144:145], v[94:97], off offset:3072
	v_cvt_pk_f16_f32 v81, v76, v77
	v_cvt_pk_f16_f32 v126, v126, v127
	v_cvt_pk_f16_f32 v127, v128, v129
	v_cvt_pk_f16_f32 v128, v122, v123
	v_cvt_pk_f16_f32 v129, v124, v125
	v_cvt_pk_f16_f32 v106, v118, v119
	v_cvt_pk_f16_f32 v107, v120, v121
	v_cvt_pk_f16_f32 v108, v114, v115
	v_cvt_pk_f16_f32 v109, v116, v117
	v_cvt_pk_f16_f32 v90, v102, v103
	v_cvt_pk_f16_f32 v91, v104, v105
	v_cvt_pk_f16_f32 v92, v98, v99
	v_cvt_pk_f16_f32 v93, v100, v101
	global_store_dwordx4 v[142:143], v[78:81], off offset:1024
	v_cvt_pk_f16_f32 v76, v82, v83
	v_cvt_pk_f16_f32 v77, v84, v85
	v_cvt_pk_f16_f32 v74, v86, v87
	v_cvt_pk_f16_f32 v75, v88, v89
	v_cvt_pk_f16_f32 v62, v62, v63
	v_cvt_pk_f16_f32 v63, v64, v65
	v_cvt_pk_f16_f32 v64, v58, v59
	v_cvt_pk_f16_f32 v65, v60, v61
	v_cvt_pk_f16_f32 v42, v54, v55
	v_cvt_pk_f16_f32 v43, v56, v57
	v_cvt_pk_f16_f32 v45, v52, v53
	v_cvt_pk_f16_f32 v26, v38, v39
	v_cvt_pk_f16_f32 v27, v40, v41
	v_cvt_pk_f16_f32 v28, v34, v35
	v_cvt_pk_f16_f32 v29, v36, v37
	v_cvt_pk_f16_f32 v10, v22, v23
	v_cvt_pk_f16_f32 v11, v24, v25
	v_cvt_pk_f16_f32 v12, v18, v19
	v_cvt_pk_f16_f32 v13, v20, v21
	v_cvt_pk_f16_f32 v6, v6, v7
	v_cvt_pk_f16_f32 v7, v8, v9
	v_cvt_pk_f16_f32 v8, v2, v3
	v_cvt_pk_f16_f32 v9, v4, v5
	s_andn2_b64 vcc, exec, s[34:35]
	s_mov_b64 s[34:35], -1
	global_store_dwordx4 v[144:145], v[126:129], off
	global_store_dwordx4 v[144:145], v[106:109], off offset:2048
	global_store_dwordx4 v[142:143], v[90:93], off
	global_store_dwordx4 v[142:143], v[74:77], off offset:2048
	global_store_dwordx4 v[142:143], v[70:73], off offset:3072
	global_store_dwordx4 v[140:141], v[62:65], off
	global_store_dwordx4 v[140:141], v[42:45], off offset:2048
	global_store_dwordx4 v[138:139], v[26:29], off
	global_store_dwordx4 v[138:139], v[10:13], off offset:2048
	global_store_dwordx4 v[138:139], v[6:9], off offset:3072
	s_cbranch_vccnz .LBB0_1124
	v_readlane_b32 s22, v253, 31
	v_readlane_b32 s23, v253, 32
	s_and_b64 vcc, exec, s[22:23]
	s_cbranch_vccnz .LBB0_1123
	s_barrier
	s_branch .LBB0_1123

; #define PG8_LAS __attribute__((address_space(3)))
;     __device__ __forceinline__ void operator()(const f32x4 (&acc)[2][2][4][2], const Unit& u, int wr, int wc, int fr, int fq) const {
;         const int br = u.pn >> 2, pc = u.pn & 3;
;         const int row0 = u.pm * BM + wr * 64 + fr; const int col0 = pc * BM + wc * 32 + 8 * fq;
;         if (br == 2) { __builtin_amdgcn_fence(__ATOMIC_ACQUIRE, "agent"); }
;         const int b = (u.pm * BM) / SEQ; float rs[2][4]; row_rstd(u, wr, fr, rs);
;         f32x4 bv[2][2];
; #pragma unroll
;         for (int bj = 0; bj < 2; ++bj)
; #pragma unroll
;             for (int n = 0; n < 2; ++n) bv[bj][n] = *(const PG8_LAS f32x4*)(uintptr_t)(CV_LDS + u.idx * 1024 + (wc * 32 + 8 * fq + bj * HALF + 4 * n) * 4);
;         f32x4 sv[2][2];
;         if constexpr (I8) {
; #pragma unroll
;             for (int bj = 0; bj < 2; ++bj)
; #pragma unroll
;                 for (int n = 0; n < 2; ++n) sv[bj][n] = *(const PG8_LAS f32x4*)(uintptr_t)(SB_LDS + u.idx * 1024 + (wc * 32 + 8 * fq + bj * HALF + 4 * n) * 4); }
;         f16* Yb = Y + (size_t)br * YSTR;
; #pragma unroll
;         for (int ai = 0; ai < 2; ++ai) {
;             const int rowa = row0 + ai * HALF; const size_t offa = (size_t)rowa * 1024 + (size_t)(rowa >> 12) * GAPY + col0;
; #pragma unroll
;             for (int mp = 0; mp < 2; ++mp) {
;             f16x8 yv[4][2];
; #pragma unroll
;             for (int m = 2 * mp; m < 2 * mp + 2; ++m)
; #pragma unroll
;                 for (int bj = 0; bj < 2; ++bj) yv[m][bj] = *(const g_f16x8*)(Yb + offa + (size_t)m * 16 * 1024 + bj * HALF);
; #pragma unroll
;             for (int m = 2 * mp; m < 2 * mp + 2; ++m) { const size_t off = offa + (size_t)m * 16 * 1024;
;                 f16x8 za[2], zb[2];
;                 if (br == 2) {
; #pragma unroll
;                     for (int bj = 0; bj < 2; ++bj) { za[bj] = *(const g_f16x8*)(Y + off + bj * HALF); zb[bj] = *(const g_f16x8*)(Y + YSTR + off + bj * HALF); } }
.LBB0_1228:
	s_lshl_b32 s37, s47, 8
	s_and_b32 s37, s37, 0x300
	v_lshl_add_u32 v218, s26, 8, v208
	v_add_u32_e32 v216, s37, v237
	s_lshl_b32 s46, s46, 10
	s_ashr_i32 s37, s36, 31
	v_ashrrev_i32_e32 v219, 31, v218
	s_add_i32 s47, s46, s87
	s_lshl_b64 s[36:37], s[36:37], 23
	v_ashrrev_i32_e32 v217, 31, v216
	v_lshlrev_b64 v[26:27], 10, v[218:219]
	s_add_u32 s48, s40, s36
	v_ashrrev_i32_e32 v28, 12, v218
	v_lshl_add_u64 v[26:27], v[26:27], 0, v[216:217]
	s_mov_b32 s26, 0xc00000
	s_addc_u32 s49, s41, s37
	v_mad_i64_i32 v[228:229], s[36:37], v28, s26, v[26:27]
	v_and_b32_e32 v238, 15, v218
	v_lshlrev_b32_e32 v238, 4, v238
	v_bfe_u32 v26, v216, 3, 2
	v_lshl_or_b32 v238, v26, 8, v238
	v_bfe_u32 v26, v216, 5, 2
	v_lshl_or_b32 v238, v26, 14, v238
	v_bfe_u32 v26, v218, 6, 1
	v_lshl_or_b32 v238, v26, 16, v238
	v_lshrrev_b32_e32 v26, 8, v216
	v_lshl_add_u32 v238, v26, 17, v238
	v_lshrrev_b32_e32 v26, 8, v218
	v_lshl_add_u32 v238, v26, 19, v238
	v_lshrrev_b32_e32 v26, 12, v218
	v_mul_u32_u24_e32 v26, 3, v26
	v_lshl_add_u32 v238, v26, 23, v238
	v_mov_b32_e32 v224, v238
	v_mov_b32_e32 v225, 0
	v_lshl_add_u64 v[224:225], s[48:49], 0, v[224:225]
	v_add_co_u32_e32 v26, vcc, 0x800, v224
	global_load_dwordx4 v[190:193], v[224:225], off sc1
	global_load_dwordx4 v[186:189], v[224:225], off offset:1024 sc1
	v_addc_co_u32_e32 v27, vcc, 0, v225, vcc
	global_load_dwordx4 v[174:177], v[26:27], off sc1
	global_load_dwordx4 v[162:165], v[26:27], off offset:1024 sc1
	v_lshl_add_u32 v26, v197, 2, s47
	v_add_u32_e32 v26, 0x20000, v26
	ds_read2_b32 v[226:227], v26 offset1:16
	ds_read2_b32 v[220:221], v26 offset0:32 offset1:48
	ds_read2_b32 v[214:215], v26 offset0:128 offset1:144
	ds_read2_b32 v[212:213], v26 offset0:160 offset1:176
	v_add_u32_e32 v26, s46, v199
	v_add_u32_e32 v30, s46, v244
	ds_read_b128 v[62:65], v26
	ds_read_b128 v[50:53], v26 offset:16
	ds_read_b128 v[34:37], v26 offset:512
	ds_read_b128 v[26:29], v26 offset:528
	ds_read_b128 v[70:73], v30
	ds_read_b128 v[54:57], v30 offset:16
	ds_read_b128 v[38:41], v30 offset:512
	ds_read_b128 v[30:33], v30 offset:528
	v_cndmask_b32_e64 v42, 0, 1, s[38:39]
	v_cmp_ne_u32_e64 s[36:37], 1, v42
	v_bfrev_b32_e32 v211, 1
	s_andn2_b64 vcc, exec, s[38:39]
	s_cbranch_vccnz .LBB0_1230
	v_mov_b32_e32 v42, v238
	v_mov_b32_e32 v43, 0
	v_lshl_add_u64 v[44:45], s[40:41], 0, v[42:43]
	v_lshl_add_u64 v[46:47], s[44:45], 0, v[42:43]
	global_load_dwordx4 v[58:61], v[44:45], off sc1
	s_nop 0
	global_load_dwordx4 v[42:45], v[44:45], off offset:1024 sc1
	s_nop 0
	global_load_dwordx4 v[66:69], v[46:47], off sc1
	s_nop 0
	global_load_dwordx4 v[46:49], v[46:47], off offset:1024 sc1
	s_branch .LBB0_1231

; __device__ __forceinline__ unsigned pk2h(float lo, float hi) { f32x2 v = {lo, hi}; f16x2 h = __builtin_convertvector(v, f16x2); return __builtin_bit_cast(unsigned, h); }
;     __device__ __forceinline__ void operator()(const f32x4 (&acc)[2][2][4][2], const Unit& u, int wr, int wc, int fr, int fq) const {
;     ...
;                 for (int bj = 0; bj < 2; ++bj) {
;                     f32x4 a0 = acc[ai][bj][m][0], a1 = acc[ai][bj][m][1];
;                     if constexpr (I8) { const i32x4 i0 = __builtin_bit_cast(i32x4, a0), i1 = __builtin_bit_cast(i32x4, a1);
;                         a0 = (f32x4){(float)i0.x, (float)i0.y, (float)i0.z, (float)i0.w} * sv[bj][0]; a1 = (f32x4){(float)i1.x, (float)i1.y, (float)i1.z, (float)i1.w} * sv[bj][1]; }
;                     const f32x4 g0 = a0 * rs[ai][m] + bv[bj][0], g1 = a1 * rs[ai][m] + bv[bj][1];
;                     const f16x8 yy = yv[m][bj];
;                     float z[8];
; #pragma unroll
;                     for (int e = 0; e < 4; ++e) { z[e] = (float)yy[e] * __builtin_amdgcn_rcpf(1.f + __builtin_amdgcn_exp2f(-LOG2E * g0[e])); z[4 + e] = (float)yy[4 + e] * __builtin_amdgcn_rcpf(1.f + __builtin_amdgcn_exp2f(-LOG2E * g1[e])); }
;                     if (br == 2) {
; #pragma unroll
;                         for (int e = 0; e < 8; ++e) z[e] += (float)za[bj][e] + (float)zb[bj][e]; }
;                     u32x4 w; w.x = pk2h(z[0], z[1]); w.y = pk2h(z[2], z[3]); w.z = pk2h(z[4], z[5]); w.w = pk2h(z[6], z[7]);
;                     f16* dst = (br == 2) ? merged : Yb;
;                     gst16(dst + off + bj * HALF, w); } } } }
.LBB0_1234:
	v_cvt_pk_f16_f32 v192, v180, v181
	v_cvt_f32_i32_e32 v180, v172
	v_cvt_f32_i32_e32 v172, v166
	v_cvt_pk_f16_f32 v191, v182, v183
	v_cvt_f32_i32_e32 v182, v167
	v_cvt_f32_i32_e32 v170, v170
	s_waitcnt lgkmcnt(0)
	v_mul_f32_e32 v167, v30, v172
	v_fma_f32 v167, v226, v167, v26
	v_mul_f32_e32 v167, 0xbfb8aa3b, v167
	v_exp_f32_e32 v167, v167
	v_cvt_f32_i32_e32 v171, v171
	v_mul_f32_e32 v166, v38, v170
	v_fma_f32 v166, v226, v166, v34
	v_add_f32_e32 v167, 1.0, v167
	v_rcp_f32_e32 v170, v167
	v_mul_f32_e32 v167, v39, v171
	v_fma_f32 v167, v226, v167, v35
	v_mul_f32_e32 v166, 0xbfb8aa3b, v166
	v_mul_f32_e32 v167, 0xbfb8aa3b, v167
	v_exp_f32_e32 v166, v166
	v_exp_f32_e32 v167, v167
	v_mul_f32_e32 v171, v31, v182
	v_fma_f32 v171, v226, v171, v27
	v_mul_f32_e32 v171, 0xbfb8aa3b, v171
	v_add_f32_e32 v166, 1.0, v166
	v_add_f32_e32 v167, 1.0, v167
	v_exp_f32_e32 v171, v171
	v_cvt_f32_i32_e32 v181, v173
	v_rcp_f32_e32 v166, v166
	v_rcp_f32_e32 v167, v167
	s_waitcnt vmcnt(2)
	v_cvt_f32_f16_sdwa v173, v186 dst_sel:DWORD dst_unused:UNUSED_PAD src0_sel:WORD_1
	v_cvt_f32_f16_e32 v172, v186
	v_add_f32_e32 v171, 1.0, v171
	v_rcp_f32_e32 v171, v171
	v_cvt_pk_f16_f32 v190, v178, v179
	v_pk_mul_f32 v[166:167], v[166:167], v[172:173]
	v_cvt_f32_f16_sdwa v173, v188 dst_sel:DWORD dst_unused:UNUSED_PAD src0_sel:WORD_1
	v_cvt_f32_f16_e32 v172, v188
	v_cvt_pk_f16_f32 v193, v184, v185
	v_lshl_add_u64 v[178:179], v[228:229], 1, s[46:47]
	s_mov_b64 s[52:53], -1
	v_pk_mul_f32 v[170:171], v[170:171], v[172:173]
	v_mul_f32_e32 v172, v40, v180
	v_mul_f32_e32 v173, v41, v181
	v_fma_f32 v172, v226, v172, v36
	v_fma_f32 v173, v226, v173, v37
	v_mul_f32_e32 v172, 0xbfb8aa3b, v172
	v_mul_f32_e32 v173, 0xbfb8aa3b, v173
	v_exp_f32_e32 v172, v172
	v_exp_f32_e32 v173, v173
	v_cvt_f32_f16_sdwa v181, v187 dst_sel:DWORD dst_unused:UNUSED_PAD src0_sel:WORD_1
	v_cvt_f32_f16_e32 v180, v187
	v_add_f32_e32 v172, 1.0, v172
	v_add_f32_e32 v173, 1.0, v173
	v_rcp_f32_e32 v172, v172
	v_rcp_f32_e32 v173, v173
	s_andn2_b64 vcc, exec, s[50:51]
	v_mov_b32_e32 v222, v224
	v_mov_b32_e32 v223, v225
	v_cndmask_b32_e64 v222, v178, v222, s[36:37]
	v_cndmask_b32_e64 v223, v179, v223, s[36:37]
	global_store_dwordx4 v[222:223], v[190:193], off
	v_pk_mul_f32 v[172:173], v[172:173], v[180:181]
	v_cndmask_b32_e64 v180, 0, 1, s[50:51]
	v_cmp_ne_u32_e64 s[38:39], 1, v180
	s_cbranch_vccnz .LBB0_1236
	s_mov_b64 s[52:53], 0

; __device__ __forceinline__ unsigned pk2h(float lo, float hi) { f32x2 v = {lo, hi}; f16x2 h = __builtin_convertvector(v, f16x2); return __builtin_bit_cast(unsigned, h); }
;     __device__ __forceinline__ void operator()(const f32x4 (&acc)[2][2][4][2], const Unit& u, int wr, int wc, int fr, int fq) const {
;     ...
;             for (int m = 2 * mp; m < 2 * mp + 2; ++m) { const size_t off = offa + (size_t)m * 16 * 1024;
;                 f16x8 za[2], zb[2];
;                 if (br == 2) {
; #pragma unroll
;                     for (int bj = 0; bj < 2; ++bj) { za[bj] = *(const g_f16x8*)(Y + off + bj * HALF); zb[bj] = *(const g_f16x8*)(Y + YSTR + off + bj * HALF); } }
; #pragma unroll
;                 for (int bj = 0; bj < 2; ++bj) {
;                     f32x4 a0 = acc[ai][bj][m][0], a1 = acc[ai][bj][m][1];
;                     if constexpr (I8) { const i32x4 i0 = __builtin_bit_cast(i32x4, a0), i1 = __builtin_bit_cast(i32x4, a1);
;                         a0 = (f32x4){(float)i0.x, (float)i0.y, (float)i0.z, (float)i0.w} * sv[bj][0]; a1 = (f32x4){(float)i1.x, (float)i1.y, (float)i1.z, (float)i1.w} * sv[bj][1]; }
;                     const f32x4 g0 = a0 * rs[ai][m] + bv[bj][0], g1 = a1 * rs[ai][m] + bv[bj][1];
;                     const f16x8 yy = yv[m][bj];
;                     float z[8];
; #pragma unroll
;                     for (int e = 0; e < 4; ++e) { z[e] = (float)yy[e] * __builtin_amdgcn_rcpf(1.f + __builtin_amdgcn_exp2f(-LOG2E * g0[e])); z[4 + e] = (float)yy[4 + e] * __builtin_amdgcn_rcpf(1.f + __builtin_amdgcn_exp2f(-LOG2E * g1[e])); }
;                     if (br == 2) {
; #pragma unroll
;                         for (int e = 0; e < 8; ++e) z[e] += (float)za[bj][e] + (float)zb[bj][e]; }
;                     u32x4 w; w.x = pk2h(z[0], z[1]); w.y = pk2h(z[2], z[3]); w.z = pk2h(z[4], z[5]); w.w = pk2h(z[6], z[7]);
;                     f16* dst = (br == 2) ? merged : Yb;
;                     gst16(dst + off + bj * HALF, w); } } } }
.LBB0_1239:
	v_cvt_pk_f16_f32 v180, v166, v167
	v_cvt_pk_f16_f32 v181, v172, v173
	v_cvt_pk_f16_f32 v182, v170, v171
	v_cvt_pk_f16_f32 v183, v168, v169
	s_and_b64 vcc, exec, s[36:37]
	s_mov_b64 s[28:29], 0x300
	v_lshl_add_u64 v[222:223], v[224:225], 0, s[28:29]
	v_cndmask_b32_e64 v222, v178, v222, s[36:37]
	v_cndmask_b32_e64 v223, v179, v223, s[36:37]
	global_store_dwordx4 v[222:223], v[180:183], off offset:256
	s_cbranch_vccnz .LBB0_1241
	v_add_u32_e32 v42, 0x800, v238
	v_mov_b32_e32 v43, 0
	v_lshl_add_u64 v[44:45], s[40:41], 0, v[42:43]
	s_waitcnt vmcnt(2)
	v_lshl_add_u64 v[46:47], s[44:45], 0, v[42:43]
	global_load_dwordx4 v[58:61], v[44:45], off sc1
	s_nop 0
	global_load_dwordx4 v[42:45], v[44:45], off offset:1024 sc1
	s_nop 0
	global_load_dwordx4 v[66:69], v[46:47], off sc1
	s_nop 0
	global_load_dwordx4 v[46:49], v[46:47], off offset:1024 sc1

; __device__ __forceinline__ unsigned pk2h(float lo, float hi) { f32x2 v = {lo, hi}; f16x2 h = __builtin_convertvector(v, f16x2); return __builtin_bit_cast(unsigned, h); }
;     __device__ __forceinline__ void operator()(const f32x4 (&acc)[2][2][4][2], const Unit& u, int wr, int wc, int fr, int fq) const {
;     ...
;                 for (int bj = 0; bj < 2; ++bj) {
;                     f32x4 a0 = acc[ai][bj][m][0], a1 = acc[ai][bj][m][1];
;                     if constexpr (I8) { const i32x4 i0 = __builtin_bit_cast(i32x4, a0), i1 = __builtin_bit_cast(i32x4, a1);
;                         a0 = (f32x4){(float)i0.x, (float)i0.y, (float)i0.z, (float)i0.w} * sv[bj][0]; a1 = (f32x4){(float)i1.x, (float)i1.y, (float)i1.z, (float)i1.w} * sv[bj][1]; }
;                     const f32x4 g0 = a0 * rs[ai][m] + bv[bj][0], g1 = a1 * rs[ai][m] + bv[bj][1];
;                     const f16x8 yy = yv[m][bj];
;                     float z[8];
; #pragma unroll
;                     for (int e = 0; e < 4; ++e) { z[e] = (float)yy[e] * __builtin_amdgcn_rcpf(1.f + __builtin_amdgcn_exp2f(-LOG2E * g0[e])); z[4 + e] = (float)yy[4 + e] * __builtin_amdgcn_rcpf(1.f + __builtin_amdgcn_exp2f(-LOG2E * g1[e])); }
;                     if (br == 2) {
; #pragma unroll
;                         for (int e = 0; e < 8; ++e) z[e] += (float)za[bj][e] + (float)zb[bj][e]; }
;                     u32x4 w; w.x = pk2h(z[0], z[1]); w.y = pk2h(z[2], z[3]); w.z = pk2h(z[4], z[5]); w.w = pk2h(z[6], z[7]);
;                     f16* dst = (br == 2) ? merged : Yb;
;                     gst16(dst + off + bj * HALF, w); } } } }
.LBB0_1243:
	s_mov_b32 s26, 0x8000
	v_cvt_pk_f16_f32 v154, v154, v155
	v_cvt_pk_f16_f32 v155, v158, v159
	v_add_co_u32_e32 v158, vcc, s26, v178
	v_cvt_pk_f16_f32 v156, v156, v157
	v_cvt_pk_f16_f32 v157, v160, v161
	v_addc_co_u32_e32 v159, vcc, 0, v179, vcc
	s_mov_b64 s[28:29], 0x800
	v_lshl_add_u64 v[222:223], v[224:225], 0, s[28:29]
	v_cndmask_b32_e64 v222, v158, v222, s[36:37]
	v_cndmask_b32_e64 v223, v159, v223, s[36:37]
	global_store_dwordx4 v[222:223], v[154:157], off
	v_cvt_f32_i32_e32 v150, v150
	v_cvt_f32_i32_e32 v151, v151
	v_cvt_f32_i32_e32 v154, v152
	v_cvt_f32_i32_e32 v152, v146
	v_cvt_f32_i32_e32 v156, v147
	v_mul_f32_e32 v146, v38, v150
	v_fma_f32 v146, v227, v146, v34
	v_mul_f32_e32 v147, v30, v152
	v_fma_f32 v147, v227, v147, v26
	v_mul_f32_e32 v147, 0xbfb8aa3b, v147
	v_exp_f32_e32 v147, v147
	v_mul_f32_e32 v146, 0xbfb8aa3b, v146
	v_exp_f32_e32 v146, v146
	v_cvt_f32_i32_e32 v155, v153
	v_add_f32_e32 v147, 1.0, v147
	v_rcp_f32_e32 v150, v147
	v_mul_f32_e32 v147, v39, v151
	v_fma_f32 v147, v227, v147, v35
	v_mul_f32_e32 v147, 0xbfb8aa3b, v147
	v_exp_f32_e32 v147, v147
	v_mul_f32_e32 v151, v31, v156
	v_fma_f32 v151, v227, v151, v27
	v_mul_f32_e32 v151, 0xbfb8aa3b, v151
	v_add_f32_e32 v146, 1.0, v146
	v_add_f32_e32 v147, 1.0, v147
	v_exp_f32_e32 v151, v151
	v_rcp_f32_e32 v146, v146
	v_rcp_f32_e32 v147, v147
	s_waitcnt vmcnt(3)
	v_cvt_f32_f16_sdwa v153, v162 dst_sel:DWORD dst_unused:UNUSED_PAD src0_sel:WORD_1
	v_cvt_f32_f16_e32 v152, v162
	v_add_f32_e32 v151, 1.0, v151
	v_rcp_f32_e32 v151, v151
	s_mov_b64 s[50:51], -1
	v_pk_mul_f32 v[146:147], v[146:147], v[152:153]
	v_cvt_f32_f16_sdwa v153, v164 dst_sel:DWORD dst_unused:UNUSED_PAD src0_sel:WORD_1
	v_cvt_f32_f16_e32 v152, v164
	s_and_b64 vcc, exec, s[38:39]
	v_pk_mul_f32 v[150:151], v[150:151], v[152:153]
	v_mul_f32_e32 v152, v40, v154
	v_mul_f32_e32 v153, v41, v155
	v_fma_f32 v152, v227, v152, v36
	v_fma_f32 v153, v227, v153, v37
	v_mul_f32_e32 v152, 0xbfb8aa3b, v152
	v_mul_f32_e32 v153, 0xbfb8aa3b, v153
	v_exp_f32_e32 v152, v152
	v_exp_f32_e32 v153, v153
	v_cvt_f32_f16_sdwa v155, v163 dst_sel:DWORD dst_unused:UNUSED_PAD src0_sel:WORD_1
	v_cvt_f32_f16_e32 v154, v163
	v_add_f32_e32 v152, 1.0, v152
	v_add_f32_e32 v153, 1.0, v153
	v_rcp_f32_e32 v152, v152
	v_rcp_f32_e32 v153, v153
	s_nop 0
	v_pk_mul_f32 v[152:153], v[152:153], v[154:155]
	s_cbranch_vccnz .LBB0_1245
	s_mov_b64 s[50:51], 0

; __device__ __forceinline__ unsigned pk2h(float lo, float hi) { f32x2 v = {lo, hi}; f16x2 h = __builtin_convertvector(v, f16x2); return __builtin_bit_cast(unsigned, h); }
;     __device__ __forceinline__ void operator()(const f32x4 (&acc)[2][2][4][2], const Unit& u, int wr, int wc, int fr, int fq) const {
;     ...
;             for (int mp = 0; mp < 2; ++mp) {
;             f16x8 yv[4][2];
; #pragma unroll
;             for (int m = 2 * mp; m < 2 * mp + 2; ++m)
; #pragma unroll
;                 for (int bj = 0; bj < 2; ++bj) yv[m][bj] = *(const g_f16x8*)(Yb + offa + (size_t)m * 16 * 1024 + bj * HALF);
; #pragma unroll
;             for (int m = 2 * mp; m < 2 * mp + 2; ++m) { const size_t off = offa + (size_t)m * 16 * 1024;
;                 f16x8 za[2], zb[2];
;                 if (br == 2) {
; #pragma unroll
;                     for (int bj = 0; bj < 2; ++bj) { za[bj] = *(const g_f16x8*)(Y + off + bj * HALF); zb[bj] = *(const g_f16x8*)(Y + YSTR + off + bj * HALF); } }
; #pragma unroll
;                 for (int bj = 0; bj < 2; ++bj) {
;                     f32x4 a0 = acc[ai][bj][m][0], a1 = acc[ai][bj][m][1];
;                     if constexpr (I8) { const i32x4 i0 = __builtin_bit_cast(i32x4, a0), i1 = __builtin_bit_cast(i32x4, a1);
;                         a0 = (f32x4){(float)i0.x, (float)i0.y, (float)i0.z, (float)i0.w} * sv[bj][0]; a1 = (f32x4){(float)i1.x, (float)i1.y, (float)i1.z, (float)i1.w} * sv[bj][1]; }
;                     const f32x4 g0 = a0 * rs[ai][m] + bv[bj][0], g1 = a1 * rs[ai][m] + bv[bj][1];
;                     const f16x8 yy = yv[m][bj];
;                     float z[8];
; #pragma unroll
;                     for (int e = 0; e < 4; ++e) { z[e] = (float)yy[e] * __builtin_amdgcn_rcpf(1.f + __builtin_amdgcn_exp2f(-LOG2E * g0[e])); z[4 + e] = (float)yy[4 + e] * __builtin_amdgcn_rcpf(1.f + __builtin_amdgcn_exp2f(-LOG2E * g1[e])); }
;                     if (br == 2) {
; #pragma unroll
;                         for (int e = 0; e < 8; ++e) z[e] += (float)za[bj][e] + (float)zb[bj][e]; }
;                     u32x4 w; w.x = pk2h(z[0], z[1]); w.y = pk2h(z[2], z[3]); w.z = pk2h(z[4], z[5]); w.w = pk2h(z[6], z[7]);
;                     f16* dst = (br == 2) ? merged : Yb;
;                     gst16(dst + off + bj * HALF, w); } } } }
.LBB0_1247:
	s_mov_b64 s[28:29], 0x8000
	v_lshl_add_u64 v[158:159], v[178:179], 0, s[28:29]
	v_cvt_pk_f16_f32 v154, v146, v147
	v_cvt_pk_f16_f32 v155, v152, v153
	v_cvt_pk_f16_f32 v156, v150, v151
	v_cvt_pk_f16_f32 v157, v148, v149
	v_add_co_u32_e32 v146, vcc, 0x1000, v224
	s_mov_b64 s[28:29], 0xb00
	v_lshl_add_u64 v[222:223], v[224:225], 0, s[28:29]
	v_cndmask_b32_e64 v222, v158, v222, s[36:37]
	v_cndmask_b32_e64 v223, v159, v223, s[36:37]
	global_store_dwordx4 v[222:223], v[154:157], off offset:256
	s_nop 0
	v_addc_co_u32_e32 v147, vcc, 0, v225, vcc
	global_load_dwordx4 v[158:161], v[146:147], off sc1
	global_load_dwordx4 v[154:157], v[146:147], off offset:1024 sc1
	v_add_co_u32_e32 v146, vcc, 0x1800, v224
	s_nop 1
	v_addc_co_u32_e32 v147, vcc, 0, v225, vcc
	global_load_dwordx4 v[150:153], v[146:147], off sc1
	s_nop 0
	global_load_dwordx4 v[146:149], v[146:147], off offset:1024 sc1
	s_and_b64 vcc, exec, s[36:37]
	s_cbranch_vccnz .LBB0_1249
	v_add_u32_e32 v42, 0x1000, v238
	v_mov_b32_e32 v43, 0
	v_lshl_add_u64 v[44:45], s[40:41], 0, v[42:43]
	s_waitcnt vmcnt(6)
	v_lshl_add_u64 v[46:47], s[44:45], 0, v[42:43]
	global_load_dwordx4 v[58:61], v[44:45], off sc1
	s_nop 0
	global_load_dwordx4 v[42:45], v[44:45], off offset:1024 sc1
	s_nop 0
	global_load_dwordx4 v[66:69], v[46:47], off sc1
	s_nop 0
	global_load_dwordx4 v[46:49], v[46:47], off offset:1024 sc1

; __device__ __forceinline__ unsigned pk2h(float lo, float hi) { f32x2 v = {lo, hi}; f16x2 h = __builtin_convertvector(v, f16x2); return __builtin_bit_cast(unsigned, h); }
;     __device__ __forceinline__ void operator()(const f32x4 (&acc)[2][2][4][2], const Unit& u, int wr, int wc, int fr, int fq) const {
;     ...
;                 for (int bj = 0; bj < 2; ++bj) {
;                     f32x4 a0 = acc[ai][bj][m][0], a1 = acc[ai][bj][m][1];
;                     if constexpr (I8) { const i32x4 i0 = __builtin_bit_cast(i32x4, a0), i1 = __builtin_bit_cast(i32x4, a1);
;                         a0 = (f32x4){(float)i0.x, (float)i0.y, (float)i0.z, (float)i0.w} * sv[bj][0]; a1 = (f32x4){(float)i1.x, (float)i1.y, (float)i1.z, (float)i1.w} * sv[bj][1]; }
;                     const f32x4 g0 = a0 * rs[ai][m] + bv[bj][0], g1 = a1 * rs[ai][m] + bv[bj][1];
;                     const f16x8 yy = yv[m][bj];
;                     float z[8];
; #pragma unroll
;                     for (int e = 0; e < 4; ++e) { z[e] = (float)yy[e] * __builtin_amdgcn_rcpf(1.f + __builtin_amdgcn_exp2f(-LOG2E * g0[e])); z[4 + e] = (float)yy[4 + e] * __builtin_amdgcn_rcpf(1.f + __builtin_amdgcn_exp2f(-LOG2E * g1[e])); }
;                     if (br == 2) {
; #pragma unroll
;                         for (int e = 0; e < 8; ++e) z[e] += (float)za[bj][e] + (float)zb[bj][e]; }
;                     u32x4 w; w.x = pk2h(z[0], z[1]); w.y = pk2h(z[2], z[3]); w.z = pk2h(z[4], z[5]); w.w = pk2h(z[6], z[7]);
;                     f16* dst = (br == 2) ? merged : Yb;
;                     gst16(dst + off + bj * HALF, w); } } } }
.LBB0_1251:
	s_mov_b32 s26, 0x10000
	v_cvt_pk_f16_f32 v138, v138, v139
	v_cvt_pk_f16_f32 v139, v142, v143
	v_add_co_u32_e32 v142, vcc, s26, v178
	v_cvt_pk_f16_f32 v140, v140, v141
	v_cvt_pk_f16_f32 v141, v144, v145
	v_addc_co_u32_e32 v143, vcc, 0, v179, vcc
	s_mov_b64 s[28:29], 0x1000
	v_lshl_add_u64 v[222:223], v[224:225], 0, s[28:29]
	v_cndmask_b32_e64 v222, v142, v222, s[36:37]
	v_cndmask_b32_e64 v223, v143, v223, s[36:37]
	global_store_dwordx4 v[222:223], v[138:141], off
	v_cvt_f32_i32_e32 v134, v134
	v_cvt_f32_i32_e32 v135, v135
	v_cvt_f32_i32_e32 v138, v136
	v_cvt_f32_i32_e32 v136, v130
	v_cvt_f32_i32_e32 v140, v131
	v_mul_f32_e32 v130, v38, v134
	v_fma_f32 v130, v220, v130, v34
	v_mul_f32_e32 v131, v30, v136
	v_fma_f32 v131, v220, v131, v26
	v_mul_f32_e32 v131, 0xbfb8aa3b, v131
	v_exp_f32_e32 v131, v131
	v_mul_f32_e32 v130, 0xbfb8aa3b, v130
	v_exp_f32_e32 v130, v130
	v_cvt_f32_i32_e32 v139, v137
	v_add_f32_e32 v131, 1.0, v131
	v_rcp_f32_e32 v134, v131
	v_mul_f32_e32 v131, v39, v135
	v_fma_f32 v131, v220, v131, v35
	v_mul_f32_e32 v131, 0xbfb8aa3b, v131
	v_exp_f32_e32 v131, v131
	v_mul_f32_e32 v135, v31, v140
	v_fma_f32 v135, v220, v135, v27
	v_mul_f32_e32 v135, 0xbfb8aa3b, v135
	v_add_f32_e32 v130, 1.0, v130
	v_add_f32_e32 v131, 1.0, v131
	v_exp_f32_e32 v135, v135
	v_rcp_f32_e32 v130, v130
	v_rcp_f32_e32 v131, v131
	s_waitcnt vmcnt(3)
	v_cvt_f32_f16_sdwa v137, v154 dst_sel:DWORD dst_unused:UNUSED_PAD src0_sel:WORD_1
	v_cvt_f32_f16_e32 v136, v154
	v_add_f32_e32 v135, 1.0, v135
	v_rcp_f32_e32 v135, v135
	s_mov_b64 s[50:51], -1
	v_pk_mul_f32 v[130:131], v[130:131], v[136:137]
	v_cvt_f32_f16_sdwa v137, v156 dst_sel:DWORD dst_unused:UNUSED_PAD src0_sel:WORD_1
	v_cvt_f32_f16_e32 v136, v156
	s_and_b64 vcc, exec, s[38:39]
	v_pk_mul_f32 v[134:135], v[134:135], v[136:137]
	v_mul_f32_e32 v136, v40, v138
	v_mul_f32_e32 v137, v41, v139
	v_fma_f32 v136, v220, v136, v36
	v_fma_f32 v137, v220, v137, v37
	v_mul_f32_e32 v136, 0xbfb8aa3b, v136
	v_mul_f32_e32 v137, 0xbfb8aa3b, v137
	v_exp_f32_e32 v136, v136
	v_exp_f32_e32 v137, v137
	v_cvt_f32_f16_sdwa v139, v155 dst_sel:DWORD dst_unused:UNUSED_PAD src0_sel:WORD_1
	v_cvt_f32_f16_e32 v138, v155
	v_add_f32_e32 v136, 1.0, v136
	v_add_f32_e32 v137, 1.0, v137
	v_rcp_f32_e32 v136, v136
	v_rcp_f32_e32 v137, v137
	s_nop 0
	v_pk_mul_f32 v[136:137], v[136:137], v[138:139]
	s_cbranch_vccnz .LBB0_1253
	s_mov_b64 s[50:51], 0

; __device__ __forceinline__ unsigned pk2h(float lo, float hi) { f32x2 v = {lo, hi}; f16x2 h = __builtin_convertvector(v, f16x2); return __builtin_bit_cast(unsigned, h); }
;     __device__ __forceinline__ void operator()(const f32x4 (&acc)[2][2][4][2], const Unit& u, int wr, int wc, int fr, int fq) const {
;     ...
;             for (int m = 2 * mp; m < 2 * mp + 2; ++m) { const size_t off = offa + (size_t)m * 16 * 1024;
;                 f16x8 za[2], zb[2];
;                 if (br == 2) {
; #pragma unroll
;                     for (int bj = 0; bj < 2; ++bj) { za[bj] = *(const g_f16x8*)(Y + off + bj * HALF); zb[bj] = *(const g_f16x8*)(Y + YSTR + off + bj * HALF); } }
; #pragma unroll
;                 for (int bj = 0; bj < 2; ++bj) {
;                     f32x4 a0 = acc[ai][bj][m][0], a1 = acc[ai][bj][m][1];
;                     if constexpr (I8) { const i32x4 i0 = __builtin_bit_cast(i32x4, a0), i1 = __builtin_bit_cast(i32x4, a1);
;                         a0 = (f32x4){(float)i0.x, (float)i0.y, (float)i0.z, (float)i0.w} * sv[bj][0]; a1 = (f32x4){(float)i1.x, (float)i1.y, (float)i1.z, (float)i1.w} * sv[bj][1]; }
;                     const f32x4 g0 = a0 * rs[ai][m] + bv[bj][0], g1 = a1 * rs[ai][m] + bv[bj][1];
;                     const f16x8 yy = yv[m][bj];
;                     float z[8];
; #pragma unroll
;                     for (int e = 0; e < 4; ++e) { z[e] = (float)yy[e] * __builtin_amdgcn_rcpf(1.f + __builtin_amdgcn_exp2f(-LOG2E * g0[e])); z[4 + e] = (float)yy[4 + e] * __builtin_amdgcn_rcpf(1.f + __builtin_amdgcn_exp2f(-LOG2E * g1[e])); }
;                     if (br == 2) {
; #pragma unroll
;                         for (int e = 0; e < 8; ++e) z[e] += (float)za[bj][e] + (float)zb[bj][e]; }
;                     u32x4 w; w.x = pk2h(z[0], z[1]); w.y = pk2h(z[2], z[3]); w.z = pk2h(z[4], z[5]); w.w = pk2h(z[6], z[7]);
;                     f16* dst = (br == 2) ? merged : Yb;
;                     gst16(dst + off + bj * HALF, w); } } } }
.LBB0_1255:
	s_mov_b64 s[28:29], 0x10000
	v_lshl_add_u64 v[142:143], v[178:179], 0, s[28:29]
	v_cvt_pk_f16_f32 v138, v130, v131
	v_cvt_pk_f16_f32 v139, v136, v137
	v_cvt_pk_f16_f32 v140, v134, v135
	v_cvt_pk_f16_f32 v141, v132, v133
	s_and_b64 vcc, exec, s[36:37]
	s_mov_b64 s[28:29], 0x1300
	v_lshl_add_u64 v[222:223], v[224:225], 0, s[28:29]
	v_cndmask_b32_e64 v222, v142, v222, s[36:37]
	v_cndmask_b32_e64 v223, v143, v223, s[36:37]
	global_store_dwordx4 v[222:223], v[138:141], off offset:256
	s_cbranch_vccnz .LBB0_1257
	v_add_u32_e32 v42, 0x1800, v238
	v_mov_b32_e32 v43, 0
	v_lshl_add_u64 v[44:45], s[40:41], 0, v[42:43]
	s_waitcnt vmcnt(2)
	v_lshl_add_u64 v[46:47], s[44:45], 0, v[42:43]
	global_load_dwordx4 v[58:61], v[44:45], off sc1
	s_nop 0
	global_load_dwordx4 v[42:45], v[44:45], off offset:1024 sc1
	s_nop 0
	global_load_dwordx4 v[66:69], v[46:47], off sc1
	s_nop 0
	global_load_dwordx4 v[46:49], v[46:47], off offset:1024 sc1

; __device__ __forceinline__ unsigned pk2h(float lo, float hi) { f32x2 v = {lo, hi}; f16x2 h = __builtin_convertvector(v, f16x2); return __builtin_bit_cast(unsigned, h); }
;     __device__ __forceinline__ void operator()(const f32x4 (&acc)[2][2][4][2], const Unit& u, int wr, int wc, int fr, int fq) const {
;     ...
;                 for (int bj = 0; bj < 2; ++bj) {
;                     f32x4 a0 = acc[ai][bj][m][0], a1 = acc[ai][bj][m][1];
;                     if constexpr (I8) { const i32x4 i0 = __builtin_bit_cast(i32x4, a0), i1 = __builtin_bit_cast(i32x4, a1);
;                         a0 = (f32x4){(float)i0.x, (float)i0.y, (float)i0.z, (float)i0.w} * sv[bj][0]; a1 = (f32x4){(float)i1.x, (float)i1.y, (float)i1.z, (float)i1.w} * sv[bj][1]; }
;                     const f32x4 g0 = a0 * rs[ai][m] + bv[bj][0], g1 = a1 * rs[ai][m] + bv[bj][1];
;                     const f16x8 yy = yv[m][bj];
;                     float z[8];
; #pragma unroll
;                     for (int e = 0; e < 4; ++e) { z[e] = (float)yy[e] * __builtin_amdgcn_rcpf(1.f + __builtin_amdgcn_exp2f(-LOG2E * g0[e])); z[4 + e] = (float)yy[4 + e] * __builtin_amdgcn_rcpf(1.f + __builtin_amdgcn_exp2f(-LOG2E * g1[e])); }
;                     if (br == 2) {
; #pragma unroll
;                         for (int e = 0; e < 8; ++e) z[e] += (float)za[bj][e] + (float)zb[bj][e]; }
;                     u32x4 w; w.x = pk2h(z[0], z[1]); w.y = pk2h(z[2], z[3]); w.z = pk2h(z[4], z[5]); w.w = pk2h(z[6], z[7]);
;                     f16* dst = (br == 2) ? merged : Yb;
;                     gst16(dst + off + bj * HALF, w); } } } }
.LBB0_1259:
	s_mov_b32 s26, 0x18000
	v_cvt_pk_f16_f32 v122, v122, v123
	v_cvt_pk_f16_f32 v123, v126, v127
	v_add_co_u32_e32 v126, vcc, s26, v178
	v_cvt_pk_f16_f32 v124, v124, v125
	v_cvt_pk_f16_f32 v125, v128, v129
	v_addc_co_u32_e32 v127, vcc, 0, v179, vcc
	s_mov_b64 s[28:29], 0x1800
	v_lshl_add_u64 v[222:223], v[224:225], 0, s[28:29]
	v_cndmask_b32_e64 v222, v126, v222, s[36:37]
	v_cndmask_b32_e64 v223, v127, v223, s[36:37]
	global_store_dwordx4 v[222:223], v[122:125], off
	v_cvt_f32_i32_e32 v118, v118
	v_cvt_f32_i32_e32 v119, v119
	v_cvt_f32_i32_e32 v122, v120
	v_cvt_f32_i32_e32 v120, v114
	v_cvt_f32_i32_e32 v124, v115
	v_mul_f32_e32 v114, v38, v118
	v_fma_f32 v114, v221, v114, v34
	v_mul_f32_e32 v115, v30, v120
	v_fma_f32 v115, v221, v115, v26
	v_mul_f32_e32 v115, 0xbfb8aa3b, v115
	v_exp_f32_e32 v115, v115
	v_mul_f32_e32 v114, 0xbfb8aa3b, v114
	v_exp_f32_e32 v114, v114
	v_cvt_f32_i32_e32 v123, v121
	v_add_f32_e32 v115, 1.0, v115
	v_rcp_f32_e32 v118, v115
	v_mul_f32_e32 v115, v39, v119
	v_fma_f32 v115, v221, v115, v35
	v_mul_f32_e32 v115, 0xbfb8aa3b, v115
	v_exp_f32_e32 v115, v115
	v_mul_f32_e32 v119, v31, v124
	v_fma_f32 v119, v221, v119, v27
	v_mul_f32_e32 v119, 0xbfb8aa3b, v119
	v_add_f32_e32 v114, 1.0, v114
	v_add_f32_e32 v115, 1.0, v115
	v_exp_f32_e32 v119, v119
	v_rcp_f32_e32 v114, v114
	v_rcp_f32_e32 v115, v115
	s_waitcnt vmcnt(3)
	v_cvt_f32_f16_sdwa v121, v146 dst_sel:DWORD dst_unused:UNUSED_PAD src0_sel:WORD_1
	v_cvt_f32_f16_e32 v120, v146
	v_add_f32_e32 v119, 1.0, v119
	v_rcp_f32_e32 v119, v119
	s_mov_b64 s[50:51], -1
	v_pk_mul_f32 v[114:115], v[114:115], v[120:121]
	v_cvt_f32_f16_sdwa v121, v148 dst_sel:DWORD dst_unused:UNUSED_PAD src0_sel:WORD_1
	v_cvt_f32_f16_e32 v120, v148
	s_and_b64 vcc, exec, s[38:39]
	v_pk_mul_f32 v[118:119], v[118:119], v[120:121]
	v_mul_f32_e32 v120, v40, v122
	v_mul_f32_e32 v121, v41, v123
	v_fma_f32 v120, v221, v120, v36
	v_fma_f32 v121, v221, v121, v37
	v_mul_f32_e32 v120, 0xbfb8aa3b, v120
	v_mul_f32_e32 v121, 0xbfb8aa3b, v121
	v_exp_f32_e32 v120, v120
	v_exp_f32_e32 v121, v121
	v_cvt_f32_f16_sdwa v123, v147 dst_sel:DWORD dst_unused:UNUSED_PAD src0_sel:WORD_1
	v_cvt_f32_f16_e32 v122, v147
	v_add_f32_e32 v120, 1.0, v120
	v_add_f32_e32 v121, 1.0, v121
	v_rcp_f32_e32 v120, v120
	v_rcp_f32_e32 v121, v121
	s_nop 0
	v_pk_mul_f32 v[120:121], v[120:121], v[122:123]
	s_cbranch_vccnz .LBB0_1261
	s_mov_b64 s[50:51], 0

;     __device__ __forceinline__ void operator()(const f32x4 (&acc)[2][2][4][2], const Unit& u, int wr, int wc, int fr, int fq) const {
;     ...
;             const int rowa = row0 + ai * HALF; const size_t offa = (size_t)rowa * 1024 + (size_t)(rowa >> 12) * GAPY + col0;
; #pragma unroll
;             for (int mp = 0; mp < 2; ++mp) {
;             f16x8 yv[4][2];
; #pragma unroll
;             for (int m = 2 * mp; m < 2 * mp + 2; ++m)
; #pragma unroll
;                 for (int bj = 0; bj < 2; ++bj) yv[m][bj] = *(const g_f16x8*)(Yb + offa + (size_t)m * 16 * 1024 + bj * HALF);
; #pragma unroll
;             for (int m = 2 * mp; m < 2 * mp + 2; ++m) { const size_t off = offa + (size_t)m * 16 * 1024;
;                 f16x8 za[2], zb[2];
;                 if (br == 2) {
; #pragma unroll
;                     for (int bj = 0; bj < 2; ++bj) { za[bj] = *(const g_f16x8*)(Y + off + bj * HALF); zb[bj] = *(const g_f16x8*)(Y + YSTR + off + bj * HALF); } }
; #pragma unroll
;                 for (int bj = 0; bj < 2; ++bj) {
;                     f32x4 a0 = acc[ai][bj][m][0], a1 = acc[ai][bj][m][1];
;                     if constexpr (I8) { const i32x4 i0 = __builtin_bit_cast(i32x4, a0), i1 = __builtin_bit_cast(i32x4, a1);
;                         a0 = (f32x4){(float)i0.x, (float)i0.y, (float)i0.z, (float)i0.w} * sv[bj][0]; a1 = (f32x4){(float)i1.x, (float)i1.y, (float)i1.z, (float)i1.w} * sv[bj][1]; }
;                     const f32x4 g0 = a0 * rs[ai][m] + bv[bj][0], g1 = a1 * rs[ai][m] + bv[bj][1];
;                     const f16x8 yy = yv[m][bj];
;                     float z[8];
; #pragma unroll
;                     for (int e = 0; e < 4; ++e) { z[e] = (float)yy[e] * __builtin_amdgcn_rcpf(1.f + __builtin_amdgcn_exp2f(-LOG2E * g0[e])); z[4 + e] = (float)yy[4 + e] * __builtin_amdgcn_rcpf(1.f + __builtin_amdgcn_exp2f(-LOG2E * g1[e])); }
;                     if (br == 2) {
; #pragma unroll
;                         for (int e = 0; e < 8; ++e) z[e] += (float)za[bj][e] + (float)zb[bj][e]; }
;                     u32x4 w; w.x = pk2h(z[0], z[1]); w.y = pk2h(z[2], z[3]); w.z = pk2h(z[4], z[5]); w.w = pk2h(z[6], z[7]);
;                     f16* dst = (br == 2) ? merged : Yb;
;                     gst16(dst + off + bj * HALF, w); } } } }
.LBB0_1263:
	v_cvt_pk_f16_f32 v122, v114, v115
	v_add_u32_e32 v114, 0x80, v218
	v_ashrrev_i32_e32 v115, 31, v114
	v_cvt_pk_f16_f32 v125, v116, v117
	v_lshlrev_b64 v[116:117], 10, v[114:115]
	v_cvt_pk_f16_f32 v124, v118, v119
	v_ashrrev_i32_e32 v118, 12, v114
	v_lshl_add_u64 v[114:115], v[116:117], 0, v[216:217]
	s_mov_b32 s26, 0xc00000
	v_mad_i64_i32 v[130:131], s[50:51], v118, s26, v[114:115]
	s_mov_b64 s[28:29], 0x2000
	v_lshl_add_u64 v[132:133], v[224:225], 0, s[28:29]
	s_mov_b64 s[28:29], 0x18000
	v_lshl_add_u64 v[126:127], v[178:179], 0, s[28:29]
	v_cvt_pk_f16_f32 v123, v120, v121
	v_add_co_u32_e32 v114, vcc, 0x800, v132
	s_mov_b64 s[28:29], 0x1b00
	v_lshl_add_u64 v[222:223], v[224:225], 0, s[28:29]
	v_cndmask_b32_e64 v222, v126, v222, s[36:37]
	v_cndmask_b32_e64 v223, v127, v223, s[36:37]
	global_store_dwordx4 v[222:223], v[122:125], off offset:256
	s_nop 0
	v_addc_co_u32_e32 v115, vcc, 0, v133, vcc
	global_load_dwordx4 v[126:129], v[132:133], off sc1
	global_load_dwordx4 v[122:125], v[132:133], off offset:1024 sc1
	global_load_dwordx4 v[118:121], v[114:115], off sc1
	s_nop 0
	global_load_dwordx4 v[114:117], v[114:115], off offset:1024 sc1
	s_and_b64 vcc, exec, s[36:37]
	s_cbranch_vccnz .LBB0_1265
	v_add_u32_e32 v42, 0x2000, v238
	v_mov_b32_e32 v43, 0
	v_lshl_add_u64 v[44:45], s[40:41], 0, v[42:43]
	s_waitcnt vmcnt(6)
	v_lshl_add_u64 v[46:47], s[44:45], 0, v[42:43]
	global_load_dwordx4 v[58:61], v[44:45], off sc1
	s_nop 0
	global_load_dwordx4 v[42:45], v[44:45], off offset:1024 sc1
	s_nop 0
	global_load_dwordx4 v[66:69], v[46:47], off sc1
	s_nop 0
	global_load_dwordx4 v[46:49], v[46:47], off offset:1024 sc1

; __device__ __forceinline__ unsigned pk2h(float lo, float hi) { f32x2 v = {lo, hi}; f16x2 h = __builtin_convertvector(v, f16x2); return __builtin_bit_cast(unsigned, h); }
;     __device__ __forceinline__ void operator()(const f32x4 (&acc)[2][2][4][2], const Unit& u, int wr, int wc, int fr, int fq) const {
;     ...
;                 for (int bj = 0; bj < 2; ++bj) {
;                     f32x4 a0 = acc[ai][bj][m][0], a1 = acc[ai][bj][m][1];
;                     if constexpr (I8) { const i32x4 i0 = __builtin_bit_cast(i32x4, a0), i1 = __builtin_bit_cast(i32x4, a1);
;                         a0 = (f32x4){(float)i0.x, (float)i0.y, (float)i0.z, (float)i0.w} * sv[bj][0]; a1 = (f32x4){(float)i1.x, (float)i1.y, (float)i1.z, (float)i1.w} * sv[bj][1]; }
;                     const f32x4 g0 = a0 * rs[ai][m] + bv[bj][0], g1 = a1 * rs[ai][m] + bv[bj][1];
;                     const f16x8 yy = yv[m][bj];
;                     float z[8];
; #pragma unroll
;                     for (int e = 0; e < 4; ++e) { z[e] = (float)yy[e] * __builtin_amdgcn_rcpf(1.f + __builtin_amdgcn_exp2f(-LOG2E * g0[e])); z[4 + e] = (float)yy[4 + e] * __builtin_amdgcn_rcpf(1.f + __builtin_amdgcn_exp2f(-LOG2E * g1[e])); }
;                     if (br == 2) {
; #pragma unroll
;                         for (int e = 0; e < 8; ++e) z[e] += (float)za[bj][e] + (float)zb[bj][e]; }
;                     u32x4 w; w.x = pk2h(z[0], z[1]); w.y = pk2h(z[2], z[3]); w.z = pk2h(z[4], z[5]); w.w = pk2h(z[6], z[7]);
;                     f16* dst = (br == 2) ? merged : Yb;
;                     gst16(dst + off + bj * HALF, w); } } } }
.LBB0_1267:
	v_cvt_pk_f16_f32 v128, v108, v109
	v_cvt_f32_i32_e32 v108, v104
	v_cvt_f32_i32_e32 v104, v98
	v_cvt_pk_f16_f32 v127, v110, v111
	v_cvt_f32_i32_e32 v110, v99
	v_cvt_f32_i32_e32 v102, v102
	v_mul_f32_e32 v99, v30, v104
	v_fma_f32 v99, v214, v99, v26
	v_mul_f32_e32 v99, 0xbfb8aa3b, v99
	v_exp_f32_e32 v99, v99
	v_cvt_f32_i32_e32 v103, v103
	v_mul_f32_e32 v98, v38, v102
	v_fma_f32 v98, v214, v98, v34
	v_add_f32_e32 v99, 1.0, v99
	v_rcp_f32_e32 v102, v99
	v_mul_f32_e32 v99, v39, v103
	v_fma_f32 v99, v214, v99, v35
	v_mul_f32_e32 v98, 0xbfb8aa3b, v98
	v_mul_f32_e32 v99, 0xbfb8aa3b, v99
	v_exp_f32_e32 v98, v98
	v_exp_f32_e32 v99, v99
	v_mul_f32_e32 v103, v31, v110
	v_fma_f32 v103, v214, v103, v27
	v_mul_f32_e32 v103, 0xbfb8aa3b, v103
	v_add_f32_e32 v98, 1.0, v98
	v_add_f32_e32 v99, 1.0, v99
	v_exp_f32_e32 v103, v103
	v_cvt_f32_i32_e32 v109, v105
	v_rcp_f32_e32 v98, v98
	v_rcp_f32_e32 v99, v99
	s_waitcnt vmcnt(2)
	v_cvt_f32_f16_sdwa v105, v122 dst_sel:DWORD dst_unused:UNUSED_PAD src0_sel:WORD_1
	v_cvt_f32_f16_e32 v104, v122
	v_add_f32_e32 v103, 1.0, v103
	v_rcp_f32_e32 v103, v103
	v_cvt_pk_f16_f32 v126, v106, v107
	v_pk_mul_f32 v[98:99], v[98:99], v[104:105]
	v_cvt_f32_f16_sdwa v105, v124 dst_sel:DWORD dst_unused:UNUSED_PAD src0_sel:WORD_1
	v_cvt_f32_f16_e32 v104, v124
	v_cvt_pk_f16_f32 v129, v112, v113
	v_lshl_add_u64 v[106:107], v[130:131], 1, s[46:47]
	s_mov_b64 s[46:47], -1
	v_pk_mul_f32 v[102:103], v[102:103], v[104:105]
	v_mul_f32_e32 v104, v40, v108
	v_mul_f32_e32 v105, v41, v109
	v_fma_f32 v104, v214, v104, v36
	v_fma_f32 v105, v214, v105, v37
	v_mul_f32_e32 v104, 0xbfb8aa3b, v104
	v_mul_f32_e32 v105, 0xbfb8aa3b, v105
	v_exp_f32_e32 v104, v104
	v_exp_f32_e32 v105, v105
	v_cvt_f32_f16_sdwa v109, v123 dst_sel:DWORD dst_unused:UNUSED_PAD src0_sel:WORD_1
	v_cvt_f32_f16_e32 v108, v123
	v_add_f32_e32 v104, 1.0, v104
	v_add_f32_e32 v105, 1.0, v105
	v_rcp_f32_e32 v104, v104
	v_rcp_f32_e32 v105, v105
	s_and_b64 vcc, exec, s[38:39]
	s_mov_b64 s[28:29], 0x2000
	v_lshl_add_u64 v[222:223], v[224:225], 0, s[28:29]
	v_cndmask_b32_e64 v222, v106, v222, s[36:37]
	v_cndmask_b32_e64 v223, v107, v223, s[36:37]
	global_store_dwordx4 v[222:223], v[126:129], off
	v_pk_mul_f32 v[104:105], v[104:105], v[108:109]
	s_cbranch_vccnz .LBB0_1269
	s_mov_b64 s[46:47], 0

; __device__ __forceinline__ unsigned pk2h(float lo, float hi) { f32x2 v = {lo, hi}; f16x2 h = __builtin_convertvector(v, f16x2); return __builtin_bit_cast(unsigned, h); }
;     __device__ __forceinline__ void operator()(const f32x4 (&acc)[2][2][4][2], const Unit& u, int wr, int wc, int fr, int fq) const {
;     ...
;             for (int m = 2 * mp; m < 2 * mp + 2; ++m) { const size_t off = offa + (size_t)m * 16 * 1024;
;                 f16x8 za[2], zb[2];
;                 if (br == 2) {
; #pragma unroll
;                     for (int bj = 0; bj < 2; ++bj) { za[bj] = *(const g_f16x8*)(Y + off + bj * HALF); zb[bj] = *(const g_f16x8*)(Y + YSTR + off + bj * HALF); } }
; #pragma unroll
;                 for (int bj = 0; bj < 2; ++bj) {
;                     f32x4 a0 = acc[ai][bj][m][0], a1 = acc[ai][bj][m][1];
;                     if constexpr (I8) { const i32x4 i0 = __builtin_bit_cast(i32x4, a0), i1 = __builtin_bit_cast(i32x4, a1);
;                         a0 = (f32x4){(float)i0.x, (float)i0.y, (float)i0.z, (float)i0.w} * sv[bj][0]; a1 = (f32x4){(float)i1.x, (float)i1.y, (float)i1.z, (float)i1.w} * sv[bj][1]; }
;                     const f32x4 g0 = a0 * rs[ai][m] + bv[bj][0], g1 = a1 * rs[ai][m] + bv[bj][1];
;                     const f16x8 yy = yv[m][bj];
;                     float z[8];
; #pragma unroll
;                     for (int e = 0; e < 4; ++e) { z[e] = (float)yy[e] * __builtin_amdgcn_rcpf(1.f + __builtin_amdgcn_exp2f(-LOG2E * g0[e])); z[4 + e] = (float)yy[4 + e] * __builtin_amdgcn_rcpf(1.f + __builtin_amdgcn_exp2f(-LOG2E * g1[e])); }
;                     if (br == 2) {
; #pragma unroll
;                         for (int e = 0; e < 8; ++e) z[e] += (float)za[bj][e] + (float)zb[bj][e]; }
;                     u32x4 w; w.x = pk2h(z[0], z[1]); w.y = pk2h(z[2], z[3]); w.z = pk2h(z[4], z[5]); w.w = pk2h(z[6], z[7]);
;                     f16* dst = (br == 2) ? merged : Yb;
;                     gst16(dst + off + bj * HALF, w); } } } }
.LBB0_1271:
	v_cvt_pk_f16_f32 v108, v98, v99
	v_cvt_pk_f16_f32 v109, v104, v105
	v_cvt_pk_f16_f32 v110, v102, v103
	v_cvt_pk_f16_f32 v111, v100, v101
	s_and_b64 vcc, exec, s[36:37]
	s_mov_b64 s[28:29], 0x2300
	v_lshl_add_u64 v[222:223], v[224:225], 0, s[28:29]
	v_cndmask_b32_e64 v222, v106, v222, s[36:37]
	v_cndmask_b32_e64 v223, v107, v223, s[36:37]
	global_store_dwordx4 v[222:223], v[108:111], off offset:256
	s_cbranch_vccnz .LBB0_1273
	v_add_u32_e32 v42, 0x2800, v238
	v_mov_b32_e32 v43, 0
	v_lshl_add_u64 v[44:45], s[40:41], 0, v[42:43]
	s_waitcnt vmcnt(2)
	v_lshl_add_u64 v[46:47], s[44:45], 0, v[42:43]
	global_load_dwordx4 v[58:61], v[44:45], off sc1
	s_nop 0
	global_load_dwordx4 v[42:45], v[44:45], off offset:1024 sc1
	s_nop 0
	global_load_dwordx4 v[66:69], v[46:47], off sc1
	s_nop 0
	global_load_dwordx4 v[46:49], v[46:47], off offset:1024 sc1

; __device__ __forceinline__ unsigned pk2h(float lo, float hi) { f32x2 v = {lo, hi}; f16x2 h = __builtin_convertvector(v, f16x2); return __builtin_bit_cast(unsigned, h); }
;     __device__ __forceinline__ void operator()(const f32x4 (&acc)[2][2][4][2], const Unit& u, int wr, int wc, int fr, int fq) const {
;     ...
;                 for (int bj = 0; bj < 2; ++bj) {
;                     f32x4 a0 = acc[ai][bj][m][0], a1 = acc[ai][bj][m][1];
;                     if constexpr (I8) { const i32x4 i0 = __builtin_bit_cast(i32x4, a0), i1 = __builtin_bit_cast(i32x4, a1);
;                         a0 = (f32x4){(float)i0.x, (float)i0.y, (float)i0.z, (float)i0.w} * sv[bj][0]; a1 = (f32x4){(float)i1.x, (float)i1.y, (float)i1.z, (float)i1.w} * sv[bj][1]; }
;                     const f32x4 g0 = a0 * rs[ai][m] + bv[bj][0], g1 = a1 * rs[ai][m] + bv[bj][1];
;                     const f16x8 yy = yv[m][bj];
;                     float z[8];
; #pragma unroll
;                     for (int e = 0; e < 4; ++e) { z[e] = (float)yy[e] * __builtin_amdgcn_rcpf(1.f + __builtin_amdgcn_exp2f(-LOG2E * g0[e])); z[4 + e] = (float)yy[4 + e] * __builtin_amdgcn_rcpf(1.f + __builtin_amdgcn_exp2f(-LOG2E * g1[e])); }
;                     if (br == 2) {
; #pragma unroll
;                         for (int e = 0; e < 8; ++e) z[e] += (float)za[bj][e] + (float)zb[bj][e]; }
;                     u32x4 w; w.x = pk2h(z[0], z[1]); w.y = pk2h(z[2], z[3]); w.z = pk2h(z[4], z[5]); w.w = pk2h(z[6], z[7]);
;                     f16* dst = (br == 2) ? merged : Yb;
;                     gst16(dst + off + bj * HALF, w); } } } }
.LBB0_1275:
	s_mov_b32 s26, 0x8000
	v_cvt_pk_f16_f32 v90, v90, v91
	v_cvt_pk_f16_f32 v91, v94, v95
	v_add_co_u32_e32 v94, vcc, s26, v106
	v_cvt_pk_f16_f32 v92, v92, v93
	v_cvt_pk_f16_f32 v93, v96, v97
	v_addc_co_u32_e32 v95, vcc, 0, v107, vcc
	s_mov_b64 s[28:29], 0x2800
	v_lshl_add_u64 v[222:223], v[224:225], 0, s[28:29]
	v_cndmask_b32_e64 v222, v94, v222, s[36:37]
	v_cndmask_b32_e64 v223, v95, v223, s[36:37]
	global_store_dwordx4 v[222:223], v[90:93], off
	v_cvt_f32_i32_e32 v86, v86
	v_cvt_f32_i32_e32 v87, v87
	v_cvt_f32_i32_e32 v90, v88
	v_cvt_f32_i32_e32 v88, v82
	v_cvt_f32_i32_e32 v92, v83
	v_mul_f32_e32 v82, v38, v86
	v_fma_f32 v82, v215, v82, v34
	v_mul_f32_e32 v83, v30, v88
	v_fma_f32 v83, v215, v83, v26
	v_mul_f32_e32 v83, 0xbfb8aa3b, v83
	v_exp_f32_e32 v83, v83
	v_mul_f32_e32 v82, 0xbfb8aa3b, v82
	v_exp_f32_e32 v82, v82
	v_cvt_f32_i32_e32 v91, v89
	v_add_f32_e32 v83, 1.0, v83
	v_rcp_f32_e32 v86, v83
	v_mul_f32_e32 v83, v39, v87
	v_fma_f32 v83, v215, v83, v35
	v_mul_f32_e32 v83, 0xbfb8aa3b, v83
	v_exp_f32_e32 v83, v83
	v_mul_f32_e32 v87, v31, v92
	v_fma_f32 v87, v215, v87, v27
	v_mul_f32_e32 v87, 0xbfb8aa3b, v87
	v_add_f32_e32 v82, 1.0, v82
	v_add_f32_e32 v83, 1.0, v83
	v_exp_f32_e32 v87, v87
	v_rcp_f32_e32 v82, v82
	v_rcp_f32_e32 v83, v83
	s_waitcnt vmcnt(3)
	v_cvt_f32_f16_sdwa v89, v114 dst_sel:DWORD dst_unused:UNUSED_PAD src0_sel:WORD_1
	v_cvt_f32_f16_e32 v88, v114
	v_add_f32_e32 v87, 1.0, v87
	v_rcp_f32_e32 v87, v87
	s_mov_b64 s[46:47], -1
	v_pk_mul_f32 v[82:83], v[82:83], v[88:89]
	v_cvt_f32_f16_sdwa v89, v116 dst_sel:DWORD dst_unused:UNUSED_PAD src0_sel:WORD_1
	v_cvt_f32_f16_e32 v88, v116
	s_and_b64 vcc, exec, s[38:39]
	v_pk_mul_f32 v[86:87], v[86:87], v[88:89]
	v_mul_f32_e32 v88, v40, v90
	v_mul_f32_e32 v89, v41, v91
	v_fma_f32 v88, v215, v88, v36
	v_fma_f32 v89, v215, v89, v37
	v_mul_f32_e32 v88, 0xbfb8aa3b, v88
	v_mul_f32_e32 v89, 0xbfb8aa3b, v89
	v_exp_f32_e32 v88, v88
	v_exp_f32_e32 v89, v89
	v_cvt_f32_f16_sdwa v91, v115 dst_sel:DWORD dst_unused:UNUSED_PAD src0_sel:WORD_1
	v_cvt_f32_f16_e32 v90, v115
	v_add_f32_e32 v88, 1.0, v88
	v_add_f32_e32 v89, 1.0, v89
	v_rcp_f32_e32 v88, v88
	v_rcp_f32_e32 v89, v89
	s_nop 0
	v_pk_mul_f32 v[88:89], v[88:89], v[90:91]
	s_cbranch_vccnz .LBB0_1277
	s_mov_b64 s[46:47], 0

; __device__ __forceinline__ unsigned pk2h(float lo, float hi) { f32x2 v = {lo, hi}; f16x2 h = __builtin_convertvector(v, f16x2); return __builtin_bit_cast(unsigned, h); }
;     __device__ __forceinline__ void operator()(const f32x4 (&acc)[2][2][4][2], const Unit& u, int wr, int wc, int fr, int fq) const {
;     ...
;             for (int mp = 0; mp < 2; ++mp) {
;             f16x8 yv[4][2];
; #pragma unroll
;             for (int m = 2 * mp; m < 2 * mp + 2; ++m)
; #pragma unroll
;                 for (int bj = 0; bj < 2; ++bj) yv[m][bj] = *(const g_f16x8*)(Yb + offa + (size_t)m * 16 * 1024 + bj * HALF);
; #pragma unroll
;             for (int m = 2 * mp; m < 2 * mp + 2; ++m) { const size_t off = offa + (size_t)m * 16 * 1024;
;                 f16x8 za[2], zb[2];
;                 if (br == 2) {
; #pragma unroll
;                     for (int bj = 0; bj < 2; ++bj) { za[bj] = *(const g_f16x8*)(Y + off + bj * HALF); zb[bj] = *(const g_f16x8*)(Y + YSTR + off + bj * HALF); } }
; #pragma unroll
;                 for (int bj = 0; bj < 2; ++bj) {
;                     f32x4 a0 = acc[ai][bj][m][0], a1 = acc[ai][bj][m][1];
;                     if constexpr (I8) { const i32x4 i0 = __builtin_bit_cast(i32x4, a0), i1 = __builtin_bit_cast(i32x4, a1);
;                         a0 = (f32x4){(float)i0.x, (float)i0.y, (float)i0.z, (float)i0.w} * sv[bj][0]; a1 = (f32x4){(float)i1.x, (float)i1.y, (float)i1.z, (float)i1.w} * sv[bj][1]; }
;                     const f32x4 g0 = a0 * rs[ai][m] + bv[bj][0], g1 = a1 * rs[ai][m] + bv[bj][1];
;                     const f16x8 yy = yv[m][bj];
;                     float z[8];
; #pragma unroll
;                     for (int e = 0; e < 4; ++e) { z[e] = (float)yy[e] * __builtin_amdgcn_rcpf(1.f + __builtin_amdgcn_exp2f(-LOG2E * g0[e])); z[4 + e] = (float)yy[4 + e] * __builtin_amdgcn_rcpf(1.f + __builtin_amdgcn_exp2f(-LOG2E * g1[e])); }
;                     if (br == 2) {
; #pragma unroll
;                         for (int e = 0; e < 8; ++e) z[e] += (float)za[bj][e] + (float)zb[bj][e]; }
;                     u32x4 w; w.x = pk2h(z[0], z[1]); w.y = pk2h(z[2], z[3]); w.z = pk2h(z[4], z[5]); w.w = pk2h(z[6], z[7]);
;                     f16* dst = (br == 2) ? merged : Yb;
;                     gst16(dst + off + bj * HALF, w); } } } }
.LBB0_1279:
	s_mov_b64 s[28:29], 0x8000
	v_lshl_add_u64 v[94:95], v[106:107], 0, s[28:29]
	v_cvt_pk_f16_f32 v90, v82, v83
	v_cvt_pk_f16_f32 v91, v88, v89
	v_cvt_pk_f16_f32 v92, v86, v87
	v_cvt_pk_f16_f32 v93, v84, v85
	v_add_co_u32_e32 v82, vcc, 0x1000, v132
	s_mov_b64 s[28:29], 0x2b00
	v_lshl_add_u64 v[222:223], v[224:225], 0, s[28:29]
	v_cndmask_b32_e64 v222, v94, v222, s[36:37]
	v_cndmask_b32_e64 v223, v95, v223, s[36:37]
	global_store_dwordx4 v[222:223], v[90:93], off offset:256
	s_nop 0
	v_addc_co_u32_e32 v83, vcc, 0, v133, vcc
	global_load_dwordx4 v[94:97], v[82:83], off sc1
	global_load_dwordx4 v[90:93], v[82:83], off offset:1024 sc1
	v_add_co_u32_e32 v82, vcc, 0x1800, v132
	s_nop 1
	v_addc_co_u32_e32 v83, vcc, 0, v133, vcc
	global_load_dwordx4 v[86:89], v[82:83], off sc1
	s_nop 0
	global_load_dwordx4 v[82:85], v[82:83], off offset:1024 sc1
	s_and_b64 vcc, exec, s[36:37]
	s_cbranch_vccnz .LBB0_1281
	v_add_u32_e32 v42, 0x3000, v238
	v_mov_b32_e32 v43, 0
	v_lshl_add_u64 v[44:45], s[40:41], 0, v[42:43]
	s_waitcnt vmcnt(6)
	v_lshl_add_u64 v[46:47], s[44:45], 0, v[42:43]
	global_load_dwordx4 v[58:61], v[44:45], off sc1
	s_nop 0
	global_load_dwordx4 v[42:45], v[44:45], off offset:1024 sc1
	s_nop 0
	global_load_dwordx4 v[66:69], v[46:47], off sc1
	s_nop 0
	global_load_dwordx4 v[46:49], v[46:47], off offset:1024 sc1

; __device__ __forceinline__ unsigned pk2h(float lo, float hi) { f32x2 v = {lo, hi}; f16x2 h = __builtin_convertvector(v, f16x2); return __builtin_bit_cast(unsigned, h); }
;     __device__ __forceinline__ void operator()(const f32x4 (&acc)[2][2][4][2], const Unit& u, int wr, int wc, int fr, int fq) const {
;     ...
;                 for (int bj = 0; bj < 2; ++bj) {
;                     f32x4 a0 = acc[ai][bj][m][0], a1 = acc[ai][bj][m][1];
;                     if constexpr (I8) { const i32x4 i0 = __builtin_bit_cast(i32x4, a0), i1 = __builtin_bit_cast(i32x4, a1);
;                         a0 = (f32x4){(float)i0.x, (float)i0.y, (float)i0.z, (float)i0.w} * sv[bj][0]; a1 = (f32x4){(float)i1.x, (float)i1.y, (float)i1.z, (float)i1.w} * sv[bj][1]; }
;                     const f32x4 g0 = a0 * rs[ai][m] + bv[bj][0], g1 = a1 * rs[ai][m] + bv[bj][1];
;                     const f16x8 yy = yv[m][bj];
;                     float z[8];
; #pragma unroll
;                     for (int e = 0; e < 4; ++e) { z[e] = (float)yy[e] * __builtin_amdgcn_rcpf(1.f + __builtin_amdgcn_exp2f(-LOG2E * g0[e])); z[4 + e] = (float)yy[4 + e] * __builtin_amdgcn_rcpf(1.f + __builtin_amdgcn_exp2f(-LOG2E * g1[e])); }
;                     if (br == 2) {
; #pragma unroll
;                         for (int e = 0; e < 8; ++e) z[e] += (float)za[bj][e] + (float)zb[bj][e]; }
;                     u32x4 w; w.x = pk2h(z[0], z[1]); w.y = pk2h(z[2], z[3]); w.z = pk2h(z[4], z[5]); w.w = pk2h(z[6], z[7]);
;                     f16* dst = (br == 2) ? merged : Yb;
;                     gst16(dst + off + bj * HALF, w); } } } }
.LBB0_1283:
	s_mov_b32 s26, 0x10000
	v_cvt_pk_f16_f32 v74, v74, v75
	v_cvt_pk_f16_f32 v75, v78, v79
	v_add_co_u32_e32 v78, vcc, s26, v106
	v_cvt_pk_f16_f32 v76, v76, v77
	v_cvt_pk_f16_f32 v77, v80, v81
	v_addc_co_u32_e32 v79, vcc, 0, v107, vcc
	s_mov_b64 s[28:29], 0x3000
	v_lshl_add_u64 v[222:223], v[224:225], 0, s[28:29]
	v_cndmask_b32_e64 v222, v78, v222, s[36:37]
	v_cndmask_b32_e64 v223, v79, v223, s[36:37]
	global_store_dwordx4 v[222:223], v[74:77], off
	v_cvt_f32_i32_e32 v22, v22
	v_cvt_f32_i32_e32 v23, v23
	v_cvt_f32_i32_e32 v74, v24
	v_cvt_f32_i32_e32 v24, v18
	v_cvt_f32_i32_e32 v76, v19
	v_mul_f32_e32 v18, v38, v22
	v_fma_f32 v18, v212, v18, v34
	v_mul_f32_e32 v19, v30, v24
	v_fma_f32 v19, v212, v19, v26
	v_mul_f32_e32 v19, 0xbfb8aa3b, v19
	v_exp_f32_e32 v19, v19
	v_mul_f32_e32 v18, 0xbfb8aa3b, v18
	v_exp_f32_e32 v18, v18
	v_cvt_f32_i32_e32 v75, v25
	v_add_f32_e32 v19, 1.0, v19
	v_rcp_f32_e32 v22, v19
	v_mul_f32_e32 v19, v39, v23
	v_fma_f32 v19, v212, v19, v35
	v_mul_f32_e32 v19, 0xbfb8aa3b, v19
	v_exp_f32_e32 v19, v19
	v_mul_f32_e32 v23, v31, v76
	v_fma_f32 v23, v212, v23, v27
	v_mul_f32_e32 v23, 0xbfb8aa3b, v23
	v_add_f32_e32 v18, 1.0, v18
	v_add_f32_e32 v19, 1.0, v19
	v_exp_f32_e32 v23, v23
	v_rcp_f32_e32 v18, v18
	v_rcp_f32_e32 v19, v19
	s_waitcnt vmcnt(3)
	v_cvt_f32_f16_sdwa v25, v90 dst_sel:DWORD dst_unused:UNUSED_PAD src0_sel:WORD_1
	v_cvt_f32_f16_e32 v24, v90
	v_add_f32_e32 v23, 1.0, v23
	v_rcp_f32_e32 v23, v23
	s_mov_b64 s[46:47], -1
	v_pk_mul_f32 v[18:19], v[18:19], v[24:25]
	v_cvt_f32_f16_sdwa v25, v92 dst_sel:DWORD dst_unused:UNUSED_PAD src0_sel:WORD_1
	v_cvt_f32_f16_e32 v24, v92
	s_and_b64 vcc, exec, s[38:39]
	v_pk_mul_f32 v[22:23], v[22:23], v[24:25]
	v_mul_f32_e32 v24, v40, v74
	v_mul_f32_e32 v25, v41, v75
	v_fma_f32 v24, v212, v24, v36
	v_fma_f32 v25, v212, v25, v37
	v_mul_f32_e32 v24, 0xbfb8aa3b, v24
	v_mul_f32_e32 v25, 0xbfb8aa3b, v25
	v_exp_f32_e32 v24, v24
	v_exp_f32_e32 v25, v25
	v_cvt_f32_f16_sdwa v75, v91 dst_sel:DWORD dst_unused:UNUSED_PAD src0_sel:WORD_1
	v_cvt_f32_f16_e32 v74, v91
	v_add_f32_e32 v24, 1.0, v24
	v_add_f32_e32 v25, 1.0, v25
	v_rcp_f32_e32 v24, v24
	v_rcp_f32_e32 v25, v25
	s_nop 0
	v_pk_mul_f32 v[24:25], v[24:25], v[74:75]
	s_cbranch_vccnz .LBB0_1285
	s_mov_b64 s[46:47], 0

; __device__ __forceinline__ unsigned pk2h(float lo, float hi) { f32x2 v = {lo, hi}; f16x2 h = __builtin_convertvector(v, f16x2); return __builtin_bit_cast(unsigned, h); }
;     __device__ __forceinline__ void operator()(const f32x4 (&acc)[2][2][4][2], const Unit& u, int wr, int wc, int fr, int fq) const {
;     ...
;             for (int m = 2 * mp; m < 2 * mp + 2; ++m) { const size_t off = offa + (size_t)m * 16 * 1024;
;                 f16x8 za[2], zb[2];
;                 if (br == 2) {
; #pragma unroll
;                     for (int bj = 0; bj < 2; ++bj) { za[bj] = *(const g_f16x8*)(Y + off + bj * HALF); zb[bj] = *(const g_f16x8*)(Y + YSTR + off + bj * HALF); } }
; #pragma unroll
;                 for (int bj = 0; bj < 2; ++bj) {
;                     f32x4 a0 = acc[ai][bj][m][0], a1 = acc[ai][bj][m][1];
;                     if constexpr (I8) { const i32x4 i0 = __builtin_bit_cast(i32x4, a0), i1 = __builtin_bit_cast(i32x4, a1);
;                         a0 = (f32x4){(float)i0.x, (float)i0.y, (float)i0.z, (float)i0.w} * sv[bj][0]; a1 = (f32x4){(float)i1.x, (float)i1.y, (float)i1.z, (float)i1.w} * sv[bj][1]; }
;                     const f32x4 g0 = a0 * rs[ai][m] + bv[bj][0], g1 = a1 * rs[ai][m] + bv[bj][1];
;                     const f16x8 yy = yv[m][bj];
;                     float z[8];
; #pragma unroll
;                     for (int e = 0; e < 4; ++e) { z[e] = (float)yy[e] * __builtin_amdgcn_rcpf(1.f + __builtin_amdgcn_exp2f(-LOG2E * g0[e])); z[4 + e] = (float)yy[4 + e] * __builtin_amdgcn_rcpf(1.f + __builtin_amdgcn_exp2f(-LOG2E * g1[e])); }
;                     if (br == 2) {
; #pragma unroll
;                         for (int e = 0; e < 8; ++e) z[e] += (float)za[bj][e] + (float)zb[bj][e]; }
;                     u32x4 w; w.x = pk2h(z[0], z[1]); w.y = pk2h(z[2], z[3]); w.z = pk2h(z[4], z[5]); w.w = pk2h(z[6], z[7]);
;                     f16* dst = (br == 2) ? merged : Yb;
;                     gst16(dst + off + bj * HALF, w); } } } }
.LBB0_1287:
	s_mov_b64 s[28:29], 0x10000
	v_lshl_add_u64 v[78:79], v[106:107], 0, s[28:29]
	v_cvt_pk_f16_f32 v74, v18, v19
	v_cvt_pk_f16_f32 v75, v24, v25
	v_cvt_pk_f16_f32 v76, v22, v23
	v_cvt_pk_f16_f32 v77, v20, v21
	s_and_b64 vcc, exec, s[36:37]
	s_mov_b64 s[28:29], 0x3300
	v_lshl_add_u64 v[222:223], v[224:225], 0, s[28:29]
	v_cndmask_b32_e64 v222, v78, v222, s[36:37]
	v_cndmask_b32_e64 v223, v79, v223, s[36:37]
	global_store_dwordx4 v[222:223], v[74:77], off offset:256
	s_cbranch_vccnz .LBB0_1289
	v_add_u32_e32 v18, 0x3800, v238
	v_mov_b32_e32 v19, 0
	v_lshl_add_u64 v[20:21], s[40:41], 0, v[18:19]
	v_lshl_add_u64 v[18:19], s[44:45], 0, v[18:19]
	global_load_dwordx4 v[58:61], v[20:21], off sc1
	global_load_dwordx4 v[42:45], v[20:21], off offset:1024 sc1
	global_load_dwordx4 v[66:69], v[18:19], off sc1
	global_load_dwordx4 v[46:49], v[18:19], off offset:1024 sc1

; __device__ __forceinline__ unsigned pk2h(float lo, float hi) { f32x2 v = {lo, hi}; f16x2 h = __builtin_convertvector(v, f16x2); return __builtin_bit_cast(unsigned, h); }
;     __device__ __forceinline__ void operator()(const f32x4 (&acc)[2][2][4][2], const Unit& u, int wr, int wc, int fr, int fq) const {
;     ...
;                 for (int bj = 0; bj < 2; ++bj) {
;                     f32x4 a0 = acc[ai][bj][m][0], a1 = acc[ai][bj][m][1];
;                     if constexpr (I8) { const i32x4 i0 = __builtin_bit_cast(i32x4, a0), i1 = __builtin_bit_cast(i32x4, a1);
;                         a0 = (f32x4){(float)i0.x, (float)i0.y, (float)i0.z, (float)i0.w} * sv[bj][0]; a1 = (f32x4){(float)i1.x, (float)i1.y, (float)i1.z, (float)i1.w} * sv[bj][1]; }
;                     const f32x4 g0 = a0 * rs[ai][m] + bv[bj][0], g1 = a1 * rs[ai][m] + bv[bj][1];
;                     const f16x8 yy = yv[m][bj];
;                     float z[8];
; #pragma unroll
;                     for (int e = 0; e < 4; ++e) { z[e] = (float)yy[e] * __builtin_amdgcn_rcpf(1.f + __builtin_amdgcn_exp2f(-LOG2E * g0[e])); z[4 + e] = (float)yy[4 + e] * __builtin_amdgcn_rcpf(1.f + __builtin_amdgcn_exp2f(-LOG2E * g1[e])); }
;                     if (br == 2) {
; #pragma unroll
;                         for (int e = 0; e < 8; ++e) z[e] += (float)za[bj][e] + (float)zb[bj][e]; }
;                     u32x4 w; w.x = pk2h(z[0], z[1]); w.y = pk2h(z[2], z[3]); w.z = pk2h(z[4], z[5]); w.w = pk2h(z[6], z[7]);
;                     f16* dst = (br == 2) ? merged : Yb;
;                     gst16(dst + off + bj * HALF, w); } } } }
.LBB0_1291:
	v_cvt_f32_i32_e32 v6, v6
	v_cvt_f32_i32_e32 v7, v7
	s_mov_b32 s26, 0x18000
	v_cvt_pk_f16_f32 v10, v10, v11
	v_cvt_pk_f16_f32 v11, v14, v15
	v_add_co_u32_e32 v14, vcc, s26, v106
	v_cvt_pk_f16_f32 v12, v12, v13
	v_cvt_pk_f16_f32 v13, v16, v17
	v_addc_co_u32_e32 v15, vcc, 0, v107, vcc
	s_mov_b64 s[28:29], 0x3800
	v_lshl_add_u64 v[222:223], v[224:225], 0, s[28:29]
	v_cndmask_b32_e64 v222, v14, v222, s[36:37]
	v_cndmask_b32_e64 v223, v15, v223, s[36:37]
	global_store_dwordx4 v[222:223], v[10:13], off
	v_cvt_f32_i32_e32 v8, v8
	v_cvt_f32_i32_e32 v9, v9
	v_cvt_f32_i32_e32 v10, v2
	v_mul_f32_e32 v2, v38, v6
	v_cvt_f32_i32_e32 v11, v4
	v_mul_f32_e32 v4, v39, v7
	v_fma_f32 v2, v213, v2, v34
	v_cvt_f32_i32_e32 v6, v3
	v_fma_f32 v4, v213, v4, v35
	v_mul_f32_e32 v2, 0xbfb8aa3b, v2
	v_mul_f32_e32 v4, 0xbfb8aa3b, v4
	v_exp_f32_e32 v2, v2
	v_exp_f32_e32 v4, v4
	v_mul_f32_e32 v3, v30, v10
	v_fma_f32 v3, v213, v3, v26
	v_mul_f32_e32 v6, v31, v6
	v_mul_f32_e32 v3, 0xbfb8aa3b, v3
	v_fma_f32 v6, v213, v6, v27
	v_add_f32_e32 v2, 1.0, v2
	v_exp_f32_e32 v7, v3
	v_add_f32_e32 v3, 1.0, v4
	v_mul_f32_e32 v6, 0xbfb8aa3b, v6
	v_cvt_f32_i32_e32 v12, v5
	v_rcp_f32_e32 v2, v2
	v_rcp_f32_e32 v3, v3
	s_waitcnt vmcnt(3)
	v_cvt_f32_f16_sdwa v5, v82 dst_sel:DWORD dst_unused:UNUSED_PAD src0_sel:WORD_1
	v_cvt_f32_f16_e32 v4, v82
	v_exp_f32_e32 v10, v6
	v_mul_f32_e32 v9, v41, v9
	v_fmac_f32_e32 v37, v213, v9
	v_pk_mul_f32 v[2:3], v[2:3], v[4:5]
	v_add_f32_e32 v4, 1.0, v10
	v_mul_f32_e32 v5, v40, v8
	v_mul_f32_e32 v10, v32, v11
	v_mul_f32_e32 v11, v33, v12
	v_fma_f32 v5, v213, v5, v36
	v_fma_f32 v10, v213, v10, v28
	v_fmac_f32_e32 v29, v213, v11
	v_mul_f32_e32 v5, 0xbfb8aa3b, v5
	v_mul_f32_e32 v10, 0xbfb8aa3b, v10
	v_mul_f32_e32 v9, 0xbfb8aa3b, v37
	v_mul_f32_e32 v11, 0xbfb8aa3b, v29
	v_exp_f32_e32 v8, v5
	v_exp_f32_e32 v10, v10
	v_exp_f32_e32 v9, v9
	v_exp_f32_e32 v11, v11
	v_add_f32_e32 v6, 1.0, v7
	v_add_f32_e32 v8, 1.0, v8
	v_add_f32_e32 v10, 1.0, v10
	v_add_f32_e32 v9, 1.0, v9
	v_add_f32_e32 v11, 1.0, v11
	v_rcp_f32_e32 v6, v6
	v_rcp_f32_e32 v7, v4
	v_cvt_f32_f16_sdwa v5, v84 dst_sel:DWORD dst_unused:UNUSED_PAD src0_sel:WORD_1
	v_cvt_f32_f16_e32 v4, v84
	v_rcp_f32_e32 v8, v8
	v_rcp_f32_e32 v10, v10
	v_rcp_f32_e32 v9, v9
	v_cvt_f32_f16_sdwa v13, v83 dst_sel:DWORD dst_unused:UNUSED_PAD src0_sel:WORD_1
	v_cvt_f32_f16_e32 v12, v83
	v_rcp_f32_e32 v11, v11
	v_cvt_f32_f16_sdwa v15, v85 dst_sel:DWORD dst_unused:UNUSED_PAD src0_sel:WORD_1
	v_cvt_f32_f16_e32 v14, v85
	v_pk_mul_f32 v[4:5], v[6:7], v[4:5]
	v_pk_mul_f32 v[6:7], v[8:9], v[12:13]
	s_and_b64 vcc, exec, s[36:37]
	v_pk_mul_f32 v[8:9], v[10:11], v[14:15]
	s_cbranch_vccnz .LBB0_1293
	v_cvt_f32_f16_sdwa v11, v42 dst_sel:DWORD dst_unused:UNUSED_PAD src0_sel:WORD_1
	v_cvt_f32_f16_e32 v10, v42
	s_waitcnt vmcnt(1)
	v_cvt_f32_f16_sdwa v13, v46 dst_sel:DWORD dst_unused:UNUSED_PAD src0_sel:WORD_1
	v_cvt_f32_f16_e32 v12, v46
	v_cvt_f32_f16_sdwa v15, v43 dst_sel:DWORD dst_unused:UNUSED_PAD src0_sel:WORD_1
	v_cvt_f32_f16_e32 v14, v43
	v_cvt_f32_f16_sdwa v17, v47 dst_sel:DWORD dst_unused:UNUSED_PAD src0_sel:WORD_1
	v_cvt_f32_f16_e32 v16, v47
	v_cvt_f32_f16_sdwa v19, v44 dst_sel:DWORD dst_unused:UNUSED_PAD src0_sel:WORD_1
	v_cvt_f32_f16_e32 v18, v44
	v_cvt_f32_f16_sdwa v21, v48 dst_sel:DWORD dst_unused:UNUSED_PAD src0_sel:WORD_1
	v_cvt_f32_f16_e32 v20, v48
	v_cvt_f32_f16_sdwa v23, v45 dst_sel:DWORD dst_unused:UNUSED_PAD src0_sel:WORD_1
	v_cvt_f32_f16_e32 v22, v45
	v_cvt_f32_f16_sdwa v25, v49 dst_sel:DWORD dst_unused:UNUSED_PAD src0_sel:WORD_1
	v_cvt_f32_f16_e32 v24, v49
	v_pk_add_f32 v[10:11], v[12:13], v[10:11]
	v_pk_add_f32 v[12:13], v[16:17], v[14:15]
	v_pk_add_f32 v[14:15], v[20:21], v[18:19]
	v_pk_add_f32 v[16:17], v[24:25], v[22:23]
	v_pk_add_f32 v[2:3], v[2:3], v[10:11]
	v_pk_add_f32 v[6:7], v[6:7], v[12:13]
	v_pk_add_f32 v[4:5], v[4:5], v[14:15]
	v_pk_add_f32 v[8:9], v[8:9], v[16:17]
.LBB0_1293:
	s_mov_b64 s[28:29], 0x18000
	v_lshl_add_u64 v[10:11], v[106:107], 0, s[28:29]
	v_cvt_pk_f16_f32 v2, v2, v3
	v_cvt_pk_f16_f32 v3, v6, v7
	v_cvt_pk_f16_f32 v4, v4, v5
	v_cvt_pk_f16_f32 v5, v8, v9
	s_andn2_b64 vcc, exec, s[34:35]
	s_mov_b64 s[34:35], -1
	s_mov_b64 s[28:29], 0x3b00
	v_lshl_add_u64 v[222:223], v[224:225], 0, s[28:29]
	v_cndmask_b32_e64 v222, v10, v222, s[36:37]
	v_cndmask_b32_e64 v223, v11, v223, s[36:37]
	global_store_dwordx4 v[222:223], v[2:5], off offset:256
	s_cbranch_vccnz .LBB0_1215
	v_readlane_b32 s22, v253, 31
	v_readlane_b32 s23, v253, 32
	s_and_b64 vcc, exec, s[22:23]
	s_cbranch_vccnz .LBB0_1214
	s_barrier
	s_branch .LBB0_1214
